# speedup vs baseline: 1.0004x; 1.0004x over previous
.LBB6_26:
	s_lshl_b64 s[0:1], s[6:7], 11
	v_lshl_add_u64 v[0:1], v[160:161], 0, s[0:1]
	s_or_b32 s0, s6, 1
	s_mov_b32 s1, 0
	s_waitcnt vmcnt(0)
	s_waitcnt lgkmcnt(0)
	s_barrier
	v_mov_b32_e32 v112, v232
	v_mov_b32_e32 v113, v233
	v_mov_b32_e32 v114, v234
	v_mov_b32_e32 v115, v235
	s_lshl_b64 s[2:3], s[0:1], 11
	v_lshl_add_u64 v[2:3], v[160:161], 0, s[2:3]
	v_mov_b32_e32 v116, v240
	v_mov_b32_e32 v117, v241
	v_mov_b32_e32 v118, v242
	v_mov_b32_e32 v119, v243
	v_mov_b32_e32 v120, v236
	v_mov_b32_e32 v121, v237
	v_mov_b32_e32 v122, v238
	v_mov_b32_e32 v123, v239
	v_mov_b32_e32 v124, v244
	v_mov_b32_e32 v125, v245
	v_mov_b32_e32 v126, v246
	v_mov_b32_e32 v127, v247
	v_add_co_u32_e32 v0, vcc, 0x10000, v160
	s_mov_b32 s2, 0x3f803f80
	s_nop 0
	v_addc_co_u32_e32 v1, vcc, 0, v161, vcc
	global_load_dwordx4 v[104:107], v[0:1], off
	global_load_dwordx4 v[100:103], v[0:1], off offset:1024
	ds_read_b128 v[136:139], v158
	ds_read_b128 v[132:135], v158 offset:1024
	v_mov_b32_e32 v0, 0
	s_mov_b32 s3, s2
	v_mov_b32_e32 v1, v0
	v_mov_b32_e32 v2, v0
	v_mov_b32_e32 v3, v0
	v_mov_b32_e32 v4, v0
	v_mov_b32_e32 v5, v0
	v_mov_b32_e32 v6, v0
	v_mov_b32_e32 v7, v0
	v_mov_b32_e32 v8, v0
	v_mov_b32_e32 v9, v0
	v_mov_b32_e32 v10, v0
	v_mov_b32_e32 v11, v0
	v_mov_b32_e32 v12, v0
	v_mov_b32_e32 v13, v0
	v_mov_b32_e32 v14, v0
	v_mov_b32_e32 v15, v0
	v_mov_b32_e32 v16, v0
	v_mov_b32_e32 v17, v0
	v_mov_b32_e32 v18, v0
	v_mov_b32_e32 v19, v0
	v_mov_b32_e32 v20, v0
	v_mov_b32_e32 v21, v0
	v_mov_b32_e32 v22, v0
	v_mov_b32_e32 v23, v0
	v_mov_b32_e32 v24, v0
	v_mov_b32_e32 v25, v0
	v_mov_b32_e32 v26, v0
	v_mov_b32_e32 v27, v0
	v_mov_b32_e32 v28, v0
	v_mov_b32_e32 v29, v0
	v_mov_b32_e32 v30, v0
	v_mov_b32_e32 v31, v0
	v_lshrrev_b32_e32 v98, 7, v158
	v_lshrrev_b32_e32 v99, 8, v158
	v_xor_b32_e32 v98, v98, v99
	v_and_b32_e32 v98, 1, v98
	v_cmp_eq_u32_e32 vcc, 0, v98
	v_mov_b32_e32 v99, s2
	v_cndmask_b32_e32 v96, 0, v99, vcc
	v_mov_b32_e32 v97, v96
	v_mov_b32_e32 v98, v96
	v_mov_b32_e32 v99, v96
	v_mov_b32_e32 v144, v0
	v_mov_b32_e32 v145, v0
	v_mov_b32_e32 v146, v0
	v_mov_b32_e32 v147, v0
	v_mov_b32_e32 v140, v0
	v_mov_b32_e32 v141, v0
	v_mov_b32_e32 v142, v0
	v_mov_b32_e32 v143, v0
	s_waitcnt vmcnt(5) lgkmcnt(1)
	v_mfma_f32_32x32x16_bf16 v[48:63], v[136:139], v[112:115], 0
	s_waitcnt vmcnt(4)
	v_mfma_f32_32x32x16_bf16 v[32:47], v[136:139], v[116:119], 0
	s_waitcnt vmcnt(3) lgkmcnt(0)
	v_mfma_f32_32x32x16_bf16 v[48:63], v[132:135], v[120:123], v[48:63]
	s_waitcnt vmcnt(2)
	v_mfma_f32_32x32x16_bf16 v[32:47], v[132:135], v[124:127], v[32:47]
	v_mov_b32_e32 v180, v0
	v_mov_b32_e32 v181, v0
	v_mov_b32_e32 v182, v0
	v_mov_b32_e32 v183, v0
	v_mov_b32_e32 v184, v0
	v_mov_b32_e32 v185, v0
	v_mov_b32_e32 v186, v0
	v_mov_b32_e32 v187, v0
	v_mov_b32_e32 v76, v0
	v_mov_b32_e32 v77, v0
	v_mov_b32_e32 v78, v0
	v_mov_b32_e32 v79, v0
	v_mov_b32_e32 v168, v0
	v_mov_b32_e32 v169, v0
	v_mov_b32_e32 v170, v0
	v_mov_b32_e32 v171, v0
	v_mov_b32_e32 v248, v0
	v_mov_b32_e32 v249, v0
	v_mov_b32_e32 v250, v0
	v_mov_b32_e32 v251, v0
	ds_read_b128 v[196:199], v158 offset:2048
	ds_read_b128 v[108:111], v158 offset:3072
	s_nop 0
	s_cmp_lt_u32 s31, 4
	s_cbranch_scc1 .Lmy_prio1
	s_setprio 1
.Lmy_prio1:
.Lmy_attn_loop1:
	v_add_u32_e32 v252, s1, v158
	v_add_u32_e32 v253, 0x10800, v252
	s_waitcnt lgkmcnt(0)
	v_mfma_f32_32x32x16_bf16 v[80:95], v[196:199], v[112:115], 0
	ds_read_b128 v[128:131], v253 offset:0
	ds_read_b128 v[148:151], v253 offset:1024
	v_cvt_pk_bf16_f32 v186, v76, v77
	v_cvt_pk_bf16_f32 v187, v78, v79
	v_exp_f32_e32 v48, v48
	v_exp_f32_e32 v49, v49
	v_exp_f32_e32 v50, v50
	v_exp_f32_e32 v51, v51
	v_mfma_f32_32x32x16_bf16 v[80:95], v[108:111], v[120:123], v[80:95]
	v_exp_f32_e32 v52, v52
	v_exp_f32_e32 v53, v53
	v_exp_f32_e32 v54, v54
	v_exp_f32_e32 v55, v55
	v_cvt_pk_bf16_f32 v172, v48, v49
	v_cvt_pk_bf16_f32 v173, v50, v51
	v_mfma_f32_16x16x32_bf16 v[140:143], v[96:99], v[180:183], v[140:143]
	v_mfma_f32_32x32x16_bf16 v[0:15], v[168:171], v[180:183], v[0:15]
	v_exp_f32_e32 v56, v56
	v_exp_f32_e32 v57, v57
	v_exp_f32_e32 v58, v58
	v_exp_f32_e32 v59, v59
	v_cvt_pk_bf16_f32 v174, v52, v53
	v_cvt_pk_bf16_f32 v175, v54, v55
	v_mfma_f32_32x32x16_bf16 v[0:15], v[248:251], v[184:187], v[0:15]
	v_exp_f32_e32 v60, v60
	v_exp_f32_e32 v61, v61
	v_exp_f32_e32 v62, v62
	v_exp_f32_e32 v63, v63
	v_cvt_pk_bf16_f32 v176, v56, v57
	v_cvt_pk_bf16_f32 v177, v58, v59
	v_mfma_f32_16x16x32_bf16 v[140:143], v[96:99], v[184:187], v[140:143]
	v_mfma_f32_32x32x16_bf16 v[64:79], v[196:199], v[116:119], 0
	ds_read_b128 v[188:191], v252 offset:4096
	ds_read_b128 v[192:195], v252 offset:5120
	v_cvt_pk_bf16_f32 v178, v60, v61
	v_cvt_pk_bf16_f32 v179, v62, v63
	v_exp_f32_e32 v32, v32
	v_exp_f32_e32 v33, v33
	v_exp_f32_e32 v34, v34
	v_exp_f32_e32 v35, v35
	v_mfma_f32_32x32x16_bf16 v[64:79], v[108:111], v[124:127], v[64:79]
	v_exp_f32_e32 v36, v36
	v_exp_f32_e32 v37, v37
	v_exp_f32_e32 v38, v38
	v_exp_f32_e32 v39, v39
	v_cvt_pk_bf16_f32 v180, v32, v33
	v_cvt_pk_bf16_f32 v181, v34, v35
	v_mfma_f32_16x16x32_bf16 v[144:147], v[96:99], v[172:175], v[144:147]
	s_waitcnt lgkmcnt(2)
	v_mfma_f32_32x32x16_bf16 v[16:31], v[128:131], v[172:175], v[16:31]
	v_exp_f32_e32 v40, v40
	v_exp_f32_e32 v41, v41
	v_exp_f32_e32 v42, v42
	v_exp_f32_e32 v43, v43
	v_cvt_pk_bf16_f32 v182, v36, v37
	v_cvt_pk_bf16_f32 v183, v38, v39
	v_mfma_f32_32x32x16_bf16 v[16:31], v[148:151], v[176:179], v[16:31]
	v_exp_f32_e32 v44, v44
	v_exp_f32_e32 v45, v45
	v_exp_f32_e32 v46, v46
	v_exp_f32_e32 v47, v47
	v_cvt_pk_bf16_f32 v184, v40, v41
	v_cvt_pk_bf16_f32 v185, v42, v43
	v_mfma_f32_16x16x32_bf16 v[144:147], v[96:99], v[176:179], v[144:147]
	s_waitcnt lgkmcnt(0)
	v_mfma_f32_32x32x16_bf16 v[48:63], v[188:191], v[112:115], 0
	ds_read_b128 v[168:171], v253 offset:2048
	ds_read_b128 v[248:251], v253 offset:3072
	v_cvt_pk_bf16_f32 v186, v44, v45
	v_cvt_pk_bf16_f32 v187, v46, v47
	v_exp_f32_e32 v80, v80
	v_exp_f32_e32 v81, v81
	v_exp_f32_e32 v82, v82
	v_exp_f32_e32 v83, v83
	v_mfma_f32_32x32x16_bf16 v[48:63], v[192:195], v[120:123], v[48:63]
	v_exp_f32_e32 v84, v84
	v_exp_f32_e32 v85, v85
	v_exp_f32_e32 v86, v86
	v_exp_f32_e32 v87, v87
	v_cvt_pk_bf16_f32 v172, v80, v81
	v_cvt_pk_bf16_f32 v173, v82, v83
	v_mfma_f32_16x16x32_bf16 v[140:143], v[96:99], v[180:183], v[140:143]
	v_mfma_f32_32x32x16_bf16 v[0:15], v[128:131], v[180:183], v[0:15]
	v_exp_f32_e32 v88, v88
	v_exp_f32_e32 v89, v89
	v_exp_f32_e32 v90, v90
	v_exp_f32_e32 v91, v91
	v_cvt_pk_bf16_f32 v174, v84, v85
	v_cvt_pk_bf16_f32 v175, v86, v87
	v_mfma_f32_32x32x16_bf16 v[0:15], v[148:151], v[184:187], v[0:15]
	v_exp_f32_e32 v92, v92
	v_exp_f32_e32 v93, v93
	v_exp_f32_e32 v94, v94
	v_exp_f32_e32 v95, v95
	v_cvt_pk_bf16_f32 v176, v88, v89
	v_cvt_pk_bf16_f32 v177, v90, v91
	v_mfma_f32_16x16x32_bf16 v[140:143], v[96:99], v[184:187], v[140:143]
	v_mfma_f32_32x32x16_bf16 v[32:47], v[188:191], v[116:119], 0
	ds_read_b128 v[196:199], v252 offset:6144
	ds_read_b128 v[108:111], v252 offset:7168
	v_cvt_pk_bf16_f32 v178, v92, v93
	v_cvt_pk_bf16_f32 v179, v94, v95
	v_exp_f32_e32 v64, v64
	v_exp_f32_e32 v65, v65
	v_exp_f32_e32 v66, v66
	v_exp_f32_e32 v67, v67
	v_mfma_f32_32x32x16_bf16 v[32:47], v[192:195], v[124:127], v[32:47]
	v_exp_f32_e32 v68, v68
	v_exp_f32_e32 v69, v69
	v_exp_f32_e32 v70, v70
	v_exp_f32_e32 v71, v71
	v_cvt_pk_bf16_f32 v180, v64, v65
	v_cvt_pk_bf16_f32 v181, v66, v67
	v_mfma_f32_16x16x32_bf16 v[144:147], v[96:99], v[172:175], v[144:147]
	s_waitcnt lgkmcnt(2)
	v_mfma_f32_32x32x16_bf16 v[16:31], v[168:171], v[172:175], v[16:31]
	v_exp_f32_e32 v72, v72
	v_exp_f32_e32 v73, v73
	v_exp_f32_e32 v74, v74
	v_exp_f32_e32 v75, v75
	v_cvt_pk_bf16_f32 v182, v68, v69
	v_cvt_pk_bf16_f32 v183, v70, v71
	v_mfma_f32_32x32x16_bf16 v[16:31], v[248:251], v[176:179], v[16:31]
	v_exp_f32_e32 v76, v76
	v_exp_f32_e32 v77, v77
	v_exp_f32_e32 v78, v78
	v_exp_f32_e32 v79, v79
	v_cvt_pk_bf16_f32 v184, v72, v73
	v_cvt_pk_bf16_f32 v185, v74, v75
	v_mfma_f32_16x16x32_bf16 v[144:147], v[96:99], v[176:179], v[144:147]
	s_addk_i32 s1, 0x1000
	s_cmp_lg_u32 s1, 0x10000
	s_cbranch_scc1 .Lmy_attn_loop1
	v_cvt_pk_bf16_f32 v186, v76, v77
	v_cvt_pk_bf16_f32 v187, v78, v79
	v_mfma_f32_32x32x16_bf16 v[0:15], v[168:171], v[180:183], v[0:15]
	s_nop 0
	v_mfma_f32_16x16x32_bf16 v[140:143], v[96:99], v[180:183], v[140:143]
	v_mfma_f32_32x32x16_bf16 v[0:15], v[248:251], v[184:187], v[0:15]
	s_nop 0
	s_nop 1
	v_mfma_f32_16x16x32_bf16 v[140:143], v[96:99], v[184:187], v[140:143]
	v_lshrrev_b32_e32 v60, 2, v158
	v_and_b32_e32 v60, 60, v60
	v_and_b32_e32 v61, 0x100, v158
	v_lshrrev_b32_e32 v61, 1, v61
	v_or_b32_e32 v60, v60, v61
	s_nop 4
	ds_bpermute_b32 v61, v60, v140
	ds_bpermute_b32 v62, v60, v144
	s_waitcnt lgkmcnt(0)
	v_mul_f32_e32 v140, 0.5, v61
	v_mul_f32_e32 v144, 0.5, v62
	v_mov_b32_e32 v34, 0x3f80
	v_cmp_gt_u32_e64 s[0:1], 32, v154
	v_or_b32_e32 v36, 0x20c00, v158
	s_mov_b32 s2, 0x3f803f80
	v_cndmask_b32_e64 v96, 0, v34, s[0:1]
	v_or_b32_e32 v34, 0x20800, v158
	ds_read_b128 v[108:111], v34
	ds_read_b128 v[128:131], v36
	v_exp_f32_e32 v34, v48
	v_exp_f32_e32 v35, v49
	s_mov_b32 s3, s2
	v_mov_b64_e32 v[52:53], s[2:3]
	v_exp_f32_e32 v32, v32
	v_exp_f32_e32 v33, v33
	v_mov_b32_e32 v97, 0
	v_cndmask_b32_e64 v34, 0, v34, s[0:1]
	v_cndmask_b32_e64 v35, 0, v35, s[0:1]
	v_cvt_pk_bf16_f32 v34, v34, v35
	v_mov_b32_e32 v35, v97
	v_mov_b32_e32 v36, v97
	v_mov_b32_e32 v37, v97
	s_mov_b32 s8, 0
	v_cndmask_b32_e64 v32, 0, v32, s[0:1]
	v_cndmask_b32_e64 v33, 0, v33, s[0:1]
	s_waitcnt lgkmcnt(1)
	v_mfma_f32_32x32x16_bf16 v[16:31], v[108:111], v[34:37], v[16:31]
	s_mov_b32 s9, s8
	v_cvt_pk_bf16_f32 v46, v32, v33
	v_mov_b64_e32 v[50:51], s[8:9]
	v_mov_b32_e32 v32, v46
	v_mov_b32_e32 v33, v97
	v_mov_b32_e32 v47, v97
	v_mov_b32_e32 v48, v97
	v_mfma_f32_4x4x4_16b_bf16 v[34:37], v[52:53], v[34:35], v[144:147]
	v_mov_b32_e32 v49, v97
	s_mov_b32 s10, s8
	v_mfma_f32_4x4x4_16b_bf16 v[38:41], v[52:53], v[50:51], v[34:37]
	s_mov_b32 s11, s8
	v_mfma_f32_4x4x4_16b_bf16 v[32:35], v[52:53], v[32:33], v[140:143]
	v_mov_b64_e32 v[44:45], s[10:11]
	v_mfma_f32_32x32x16_bf16 v[0:15], v[108:111], v[46:49], v[0:15]
	v_mov_b64_e32 v[42:43], s[8:9]
	s_mov_b32 s7, 0x7149f2ca
	s_mov_b32 s4, 0xda24260
	v_mov_b32_e32 v98, v97
	v_mov_b32_e32 v99, v97
	v_mfma_f32_4x4x4_16b_bf16 v[32:35], v[52:53], v[50:51], v[32:35]
	s_waitcnt lgkmcnt(0)
	v_mfma_f32_32x32x16_bf16 v[16:31], v[128:131], v[42:45], v[16:31]
	s_nop 2
	v_mbcnt_lo_u32_b32 v33, -1, 0
	v_mbcnt_hi_u32_b32 v33, -1, v33
	v_and_b32_e32 v35, 64, v33
	v_xor_b32_e32 v34, 32, v33
	v_add_u32_e32 v35, 64, v35
	v_cmp_lt_i32_e32 vcc, v34, v35
	v_mfma_f32_32x32x16_bf16 v[0:15], v[128:131], v[42:45], v[0:15]
	s_nop 0
	v_cndmask_b32_e32 v33, v33, v34, vcc
	v_lshlrev_b32_e32 v165, 2, v33
	ds_bpermute_b32 v35, v165, v38
	ds_bpermute_b32 v34, v165, v32
	v_mov_b32_e32 v33, v38
	s_waitcnt lgkmcnt(0)
	v_pk_add_f32 v[34:35], v[32:33], v[34:35]
	s_nop 0
	v_cmp_ngt_f32_e32 vcc, s7, v35
	v_cmp_nlt_f32_e64 s[2:3], s4, v34
	v_cmp_nlt_f32_e64 s[4:5], s4, v35
	s_or_b64 s[4:5], s[4:5], vcc
	v_cmp_ngt_f32_e32 vcc, s7, v34
	s_or_b64 s[2:3], s[2:3], vcc
	s_or_b64 vcc, s[4:5], s[2:3]
	s_cbranch_vccnz .LBB6_40

.LBB6_34:
	s_or_b64 exec, exec, s[4:5]
	s_or_b32 s26, s6, 2
	s_mov_b32 s27, 0
	s_lshl_b64 s[4:5], s[26:27], 11
	s_waitcnt lgkmcnt(0)
	v_lshl_add_u64 v[0:1], v[160:161], 0, s[4:5]
	s_or_b32 s4, s6, 3
	s_mov_b32 s5, s27
	v_mov_b32_e32 v100, v216
	v_mov_b32_e32 v101, v217
	v_mov_b32_e32 v102, v218
	v_mov_b32_e32 v103, v219
	s_lshl_b64 s[4:5], s[4:5], 11
	v_lshl_add_u64 v[2:3], v[160:161], 0, s[4:5]
	v_mov_b32_e32 v104, v224
	v_mov_b32_e32 v105, v225
	v_mov_b32_e32 v106, v226
	v_mov_b32_e32 v107, v227
	v_mov_b32_e32 v108, v220
	v_mov_b32_e32 v109, v221
	v_mov_b32_e32 v110, v222
	v_mov_b32_e32 v111, v223
	v_mov_b32_e32 v112, v228
	v_mov_b32_e32 v113, v229
	v_mov_b32_e32 v114, v230
	v_mov_b32_e32 v115, v231
	ds_read_b128 v[132:135], v158
	ds_read_b128 v[128:131], v158 offset:1024
	s_mov_b32 s4, 0x3f803f80
	v_mov_b32_e32 v136, 0
	s_mov_b32 s5, s4
	v_mov_b32_e32 v137, v136
	v_mov_b32_e32 v138, v136
	v_mov_b32_e32 v139, v136
	v_mov_b32_e32 v140, v136
	v_mov_b32_e32 v141, v136
	v_mov_b32_e32 v142, v136
	v_mov_b32_e32 v143, v136
	v_mov_b32_e32 v0, v136
	v_mov_b32_e32 v1, v136
	v_mov_b32_e32 v2, v136
	v_mov_b32_e32 v3, v136
	v_mov_b32_e32 v4, v136
	v_mov_b32_e32 v5, v136
	v_mov_b32_e32 v6, v136
	v_mov_b32_e32 v7, v136
	v_mov_b32_e32 v8, v136
	v_mov_b32_e32 v9, v136
	v_mov_b32_e32 v10, v136
	v_mov_b32_e32 v11, v136
	v_mov_b32_e32 v12, v136
	v_mov_b32_e32 v13, v136
	v_mov_b32_e32 v14, v136
	v_mov_b32_e32 v15, v136
	v_mov_b32_e32 v16, v136
	v_mov_b32_e32 v17, v136
	v_mov_b32_e32 v18, v136
	v_mov_b32_e32 v19, v136
	v_mov_b32_e32 v20, v136
	v_mov_b32_e32 v21, v136
	v_mov_b32_e32 v22, v136
	v_mov_b32_e32 v23, v136
	v_lshrrev_b32_e32 v118, 7, v158
	v_lshrrev_b32_e32 v119, 8, v158
	v_xor_b32_e32 v118, v118, v119
	v_and_b32_e32 v118, 1, v118
	v_cmp_eq_u32_e32 vcc, 0, v118
	v_mov_b32_e32 v119, s4
	v_cndmask_b32_e32 v116, 0, v119, vcc
	v_mov_b32_e32 v117, v116
	v_mov_b32_e32 v118, v116
	v_mov_b32_e32 v119, v116
	v_mov_b32_e32 v24, v136
	v_mov_b32_e32 v25, v136
	v_mov_b32_e32 v26, v136
	v_mov_b32_e32 v27, v136
	v_mov_b32_e32 v28, v136
	v_mov_b32_e32 v29, v136
	v_mov_b32_e32 v30, v136
	v_mov_b32_e32 v31, v136
	s_waitcnt vmcnt(3) lgkmcnt(1)
	v_mfma_f32_32x32x16_bf16 v[48:63], v[132:135], v[100:103], 0
	s_waitcnt vmcnt(2)
	v_mfma_f32_32x32x16_bf16 v[32:47], v[132:135], v[104:107], 0
	s_waitcnt vmcnt(1) lgkmcnt(0)
	v_mfma_f32_32x32x16_bf16 v[48:63], v[128:131], v[108:111], v[48:63]
	s_waitcnt vmcnt(0)
	v_mfma_f32_32x32x16_bf16 v[32:47], v[128:131], v[112:115], v[32:47]
	v_mov_b32_e32 v180, v136
	v_mov_b32_e32 v181, v136
	v_mov_b32_e32 v182, v136
	v_mov_b32_e32 v183, v136
	v_mov_b32_e32 v184, v136
	v_mov_b32_e32 v185, v136
	v_mov_b32_e32 v186, v136
	v_mov_b32_e32 v187, v136
	v_mov_b32_e32 v76, v136
	v_mov_b32_e32 v77, v136
	v_mov_b32_e32 v78, v136
	v_mov_b32_e32 v79, v136
	v_mov_b32_e32 v240, v136
	v_mov_b32_e32 v241, v136
	v_mov_b32_e32 v242, v136
	v_mov_b32_e32 v243, v136
	v_mov_b32_e32 v244, v136
	v_mov_b32_e32 v245, v136
	v_mov_b32_e32 v246, v136
	v_mov_b32_e32 v247, v136
	ds_read_b128 v[224:227], v158 offset:2048
	ds_read_b128 v[228:231], v158 offset:3072
	s_nop 0
	s_setprio 0
	s_cmp_lt_u32 s31, 4
	s_cbranch_scc0 .Lmy_prio2
	s_setprio 1
.Lmy_prio2:
.Lmy_attn_loop2:
	v_add_u32_e32 v248, s27, v158
	v_add_u32_e32 v249, 0x10800, v248
	s_waitcnt lgkmcnt(0)
	v_mfma_f32_32x32x16_bf16 v[80:95], v[224:227], v[100:103], 0
	ds_read_b128 v[232:235], v249 offset:0
	ds_read_b128 v[236:239], v249 offset:1024
	v_cvt_pk_bf16_f32 v186, v76, v77
	v_cvt_pk_bf16_f32 v187, v78, v79
	v_exp_f32_e32 v48, v48
	v_exp_f32_e32 v49, v49
	v_exp_f32_e32 v50, v50
	v_exp_f32_e32 v51, v51
	v_mfma_f32_32x32x16_bf16 v[80:95], v[228:231], v[108:111], v[80:95]
	v_exp_f32_e32 v52, v52
	v_exp_f32_e32 v53, v53
	v_exp_f32_e32 v54, v54
	v_exp_f32_e32 v55, v55
	v_cvt_pk_bf16_f32 v172, v48, v49
	v_cvt_pk_bf16_f32 v173, v50, v51
	v_mfma_f32_16x16x32_bf16 v[136:139], v[116:119], v[180:183], v[136:139]
	v_mfma_f32_32x32x16_bf16 v[0:15], v[240:243], v[180:183], v[0:15]
	v_exp_f32_e32 v56, v56
	v_exp_f32_e32 v57, v57
	v_exp_f32_e32 v58, v58
	v_exp_f32_e32 v59, v59
	v_cvt_pk_bf16_f32 v174, v52, v53
	v_cvt_pk_bf16_f32 v175, v54, v55
	v_mfma_f32_32x32x16_bf16 v[0:15], v[244:247], v[184:187], v[0:15]
	v_exp_f32_e32 v60, v60
	v_exp_f32_e32 v61, v61
	v_exp_f32_e32 v62, v62
	v_exp_f32_e32 v63, v63
	v_cvt_pk_bf16_f32 v176, v56, v57
	v_cvt_pk_bf16_f32 v177, v58, v59
	v_mfma_f32_16x16x32_bf16 v[136:139], v[116:119], v[184:187], v[136:139]
	v_mfma_f32_32x32x16_bf16 v[64:79], v[224:227], v[104:107], 0
	ds_read_b128 v[216:219], v248 offset:4096
	ds_read_b128 v[220:223], v248 offset:5120
	v_cvt_pk_bf16_f32 v178, v60, v61
	v_cvt_pk_bf16_f32 v179, v62, v63
	v_exp_f32_e32 v32, v32
	v_exp_f32_e32 v33, v33
	v_exp_f32_e32 v34, v34
	v_exp_f32_e32 v35, v35
	v_mfma_f32_32x32x16_bf16 v[64:79], v[228:231], v[112:115], v[64:79]
	v_exp_f32_e32 v36, v36
	v_exp_f32_e32 v37, v37
	v_exp_f32_e32 v38, v38
	v_exp_f32_e32 v39, v39
	v_cvt_pk_bf16_f32 v180, v32, v33
	v_cvt_pk_bf16_f32 v181, v34, v35
	v_mfma_f32_16x16x32_bf16 v[140:143], v[116:119], v[172:175], v[140:143]
	s_waitcnt lgkmcnt(2)
	v_mfma_f32_32x32x16_bf16 v[16:31], v[232:235], v[172:175], v[16:31]
	v_exp_f32_e32 v40, v40
	v_exp_f32_e32 v41, v41
	v_exp_f32_e32 v42, v42
	v_exp_f32_e32 v43, v43
	v_cvt_pk_bf16_f32 v182, v36, v37
	v_cvt_pk_bf16_f32 v183, v38, v39
	v_mfma_f32_32x32x16_bf16 v[16:31], v[236:239], v[176:179], v[16:31]
	v_exp_f32_e32 v44, v44
	v_exp_f32_e32 v45, v45
	v_exp_f32_e32 v46, v46
	v_exp_f32_e32 v47, v47
	v_cvt_pk_bf16_f32 v184, v40, v41
	v_cvt_pk_bf16_f32 v185, v42, v43
	v_mfma_f32_16x16x32_bf16 v[140:143], v[116:119], v[176:179], v[140:143]
	s_waitcnt lgkmcnt(0)
	v_mfma_f32_32x32x16_bf16 v[48:63], v[216:219], v[100:103], 0
	ds_read_b128 v[240:243], v249 offset:2048
	ds_read_b128 v[244:247], v249 offset:3072
	v_cvt_pk_bf16_f32 v186, v44, v45
	v_cvt_pk_bf16_f32 v187, v46, v47
	v_exp_f32_e32 v80, v80
	v_exp_f32_e32 v81, v81
	v_exp_f32_e32 v82, v82
	v_exp_f32_e32 v83, v83
	v_mfma_f32_32x32x16_bf16 v[48:63], v[220:223], v[108:111], v[48:63]
	v_exp_f32_e32 v84, v84
	v_exp_f32_e32 v85, v85
	v_exp_f32_e32 v86, v86
	v_exp_f32_e32 v87, v87
	v_cvt_pk_bf16_f32 v172, v80, v81
	v_cvt_pk_bf16_f32 v173, v82, v83
	v_mfma_f32_16x16x32_bf16 v[136:139], v[116:119], v[180:183], v[136:139]
	v_mfma_f32_32x32x16_bf16 v[0:15], v[232:235], v[180:183], v[0:15]
	v_exp_f32_e32 v88, v88
	v_exp_f32_e32 v89, v89
	v_exp_f32_e32 v90, v90
	v_exp_f32_e32 v91, v91
	v_cvt_pk_bf16_f32 v174, v84, v85
	v_cvt_pk_bf16_f32 v175, v86, v87
	v_mfma_f32_32x32x16_bf16 v[0:15], v[236:239], v[184:187], v[0:15]
	v_exp_f32_e32 v92, v92
	v_exp_f32_e32 v93, v93
	v_exp_f32_e32 v94, v94
	v_exp_f32_e32 v95, v95
	v_cvt_pk_bf16_f32 v176, v88, v89
	v_cvt_pk_bf16_f32 v177, v90, v91
	v_mfma_f32_16x16x32_bf16 v[136:139], v[116:119], v[184:187], v[136:139]
	v_mfma_f32_32x32x16_bf16 v[32:47], v[216:219], v[104:107], 0
	ds_read_b128 v[224:227], v248 offset:6144
	ds_read_b128 v[228:231], v248 offset:7168
	v_cvt_pk_bf16_f32 v178, v92, v93
	v_cvt_pk_bf16_f32 v179, v94, v95
	v_exp_f32_e32 v64, v64
	v_exp_f32_e32 v65, v65
	v_exp_f32_e32 v66, v66
	v_exp_f32_e32 v67, v67
	v_mfma_f32_32x32x16_bf16 v[32:47], v[220:223], v[112:115], v[32:47]
	v_exp_f32_e32 v68, v68
	v_exp_f32_e32 v69, v69
	v_exp_f32_e32 v70, v70
	v_exp_f32_e32 v71, v71
	v_cvt_pk_bf16_f32 v180, v64, v65
	v_cvt_pk_bf16_f32 v181, v66, v67
	v_mfma_f32_16x16x32_bf16 v[140:143], v[116:119], v[172:175], v[140:143]
	s_waitcnt lgkmcnt(2)
	v_mfma_f32_32x32x16_bf16 v[16:31], v[240:243], v[172:175], v[16:31]
	v_exp_f32_e32 v72, v72
	v_exp_f32_e32 v73, v73
	v_exp_f32_e32 v74, v74
	v_exp_f32_e32 v75, v75
	v_cvt_pk_bf16_f32 v182, v68, v69
	v_cvt_pk_bf16_f32 v183, v70, v71
	v_mfma_f32_32x32x16_bf16 v[16:31], v[244:247], v[176:179], v[16:31]
	v_exp_f32_e32 v76, v76
	v_exp_f32_e32 v77, v77
	v_exp_f32_e32 v78, v78
	v_exp_f32_e32 v79, v79
	v_cvt_pk_bf16_f32 v184, v72, v73
	v_cvt_pk_bf16_f32 v185, v74, v75
	v_mfma_f32_16x16x32_bf16 v[140:143], v[116:119], v[176:179], v[140:143]
	s_addk_i32 s27, 0x1000
	s_cmp_lg_u32 s27, 0x10000
	s_cbranch_scc1 .Lmy_attn_loop2
	v_cvt_pk_bf16_f32 v186, v76, v77
	v_cvt_pk_bf16_f32 v187, v78, v79
	v_mfma_f32_32x32x16_bf16 v[0:15], v[240:243], v[180:183], v[0:15]
	s_nop 0
	v_mfma_f32_16x16x32_bf16 v[136:139], v[116:119], v[180:183], v[136:139]
	v_mfma_f32_32x32x16_bf16 v[0:15], v[244:247], v[184:187], v[0:15]
	s_nop 0
	s_nop 1
	v_mfma_f32_16x16x32_bf16 v[136:139], v[116:119], v[184:187], v[136:139]
	s_setprio 0
	v_lshrrev_b32_e32 v60, 2, v158
	v_and_b32_e32 v60, 60, v60
	v_and_b32_e32 v61, 0x100, v158
	v_lshrrev_b32_e32 v61, 1, v61
	v_or_b32_e32 v60, v60, v61
	s_nop 4
	ds_bpermute_b32 v61, v60, v136
	ds_bpermute_b32 v62, v60, v140
	s_waitcnt lgkmcnt(0)
	v_mul_f32_e32 v136, 0.5, v61
	v_mul_f32_e32 v140, 0.5, v62
	v_or_b32_e32 v34, 0x20800, v158
	ds_read_b128 v[116:119], v34
	v_or_b32_e32 v36, 0x20c00, v158
	s_mov_b32 s4, 0x3f803f80
	v_exp_f32_e32 v35, v49
	ds_read_b128 v[120:123], v36
	v_exp_f32_e32 v34, v48
	s_mov_b32 s5, s4
	v_mov_b64_e32 v[46:47], s[4:5]
	v_exp_f32_e32 v38, v32
	v_exp_f32_e32 v39, v33
	v_cndmask_b32_e64 v34, 0, v34, s[0:1]
	v_cndmask_b32_e64 v35, 0, v35, s[0:1]
	v_mov_b32_e32 v125, 0
	v_cvt_pk_bf16_f32 v124, v34, v35
	v_mov_b32_e32 v126, v125
	v_mov_b32_e32 v127, v125
	v_cndmask_b32_e64 v38, 0, v38, s[0:1]
	v_cndmask_b32_e64 v39, 0, v39, s[0:1]
	s_waitcnt lgkmcnt(1)
	v_mfma_f32_32x32x16_bf16 v[16:31], v[116:119], v[124:127], v[16:31]
	s_mov_b32 s8, 0
	s_mov_b32 s9, s8
	v_mov_b64_e32 v[36:37], s[8:9]
	s_mov_b32 s10, s8
	s_mov_b32 s11, s8
	v_mov_b64_e32 v[44:45], s[10:11]
	v_mov_b64_e32 v[42:43], s[8:9]
	v_mfma_f32_4x4x4_16b_bf16 v[32:35], v[46:47], v[124:125], v[140:143]
	v_cvt_pk_bf16_f32 v124, v38, v39
	s_waitcnt lgkmcnt(0)
	v_mfma_f32_32x32x16_bf16 v[16:31], v[120:123], v[42:45], v[16:31]
	s_mov_b32 s9, 0x7149f2ca
	s_mov_b32 s6, 0xda24260
	v_mfma_f32_32x32x16_bf16 v[0:15], v[116:119], v[124:127], v[0:15]
	v_mfma_f32_4x4x4_16b_bf16 v[38:41], v[46:47], v[36:37], v[32:35]
	v_mfma_f32_4x4x4_16b_bf16 v[32:35], v[46:47], v[124:125], v[136:139]
	v_mfma_f32_32x32x16_bf16 v[0:15], v[120:123], v[42:45], v[0:15]
	s_nop 0
	v_mfma_f32_4x4x4_16b_bf16 v[32:35], v[46:47], v[36:37], v[32:35]
	s_nop 4
	ds_bpermute_b32 v35, v165, v38
	ds_bpermute_b32 v34, v165, v32
	v_mov_b32_e32 v33, v38
	s_waitcnt lgkmcnt(0)
	v_pk_add_f32 v[34:35], v[32:33], v[34:35]
	s_nop 0
	v_cmp_ngt_f32_e32 vcc, s9, v35
	v_cmp_nlt_f32_e64 s[4:5], s6, v34
	v_cmp_nlt_f32_e64 s[6:7], s6, v35
	s_or_b64 s[6:7], s[6:7], vcc
	v_cmp_ngt_f32_e32 vcc, s9, v34
	s_or_b64 s[4:5], s[4:5], vcc
	s_or_b64 vcc, s[6:7], s[4:5]
	s_cbranch_vccnz .LBB6_64
